# DATT full-tile compute path hand-scheduled: tight MFMA chains with deep LDS prefetch of K, bias and V fragments, packed softmax
# baseline (speedup 1.0000x reference)
; #define LAS __attribute__((address_space(3)))
; __device__ __forceinline__ void datt_stream(LAS unsigned char* lds, const DattRun& c, const float C, const int wv) {
;     ...
;         if (do0) {
; #pragma unroll
;             for (int d0 = 0; d0 < 8; ++d0) { const bf16x8 b0 = *(const LAS bf16x8*)(Ks + ATT_KSWZ(r32, (d0 * 16 + hi * 8) * 2)); p0 = __builtin_amdgcn_mfma_f32_32x32x16_bf16(b0, qr[d0], p0, 0, 0, 0); } }
;         if (do1) {
; #pragma unroll
;             for (int d0 = 0; d0 < 8; ++d0) { const bf16x8 b1 = *(const LAS bf16x8*)(Ks + ATT_KSWZ(32 + r32, (d0 * 16 + hi * 8) * 2)); p1 = __builtin_amdgcn_mfma_f32_32x32x16_bf16(b1, qr[d0], p1, 0, 0, 0); } }
;         const int db = 64 * (rel - 1) - 32 * par - r32 + 4 * hi, qi = 64 * (c.a0 + pa) + 32 * par + r32; const unsigned L = (unsigned)c.L;
;         const LAS float* tb = c.tb + (db + 2 * HALFWIN);
;     ...
;         if (do0) DS_XFORM(p0, 0);
;         if (do1) DS_XFORM(p1, 32);
;     ...
;         float pmax = -__builtin_inff();
;         if (do0) {
; #pragma unroll
;             for (int r = 0; r < 16; ++r) pmax = fmaxf(pmax, p0[r]); }
;         if (do1) {
; #pragma unroll
;             for (int r = 0; r < 16; ++r) pmax = fmaxf(pmax, p1[r]); }
;         { auto rr = __builtin_amdgcn_permlane32_swap(__float_as_uint(pmax), __float_as_uint(pmax), false, false);
;           pmax = fmaxf(__uint_as_float(rr[0]), __uint_as_float(rr[1])); }
;         const float mn = fmaxf(m_reg, pmax), alpha = __builtin_amdgcn_exp2f(m_reg - mn); m_reg = mn;
.LBB0_430:
	s_cmp_eq_u32 s6, 3
	s_cbranch_scc1 .Lft0_old
	s_cmp_lg_u64 s[10:11], 0
	s_cbranch_scc1 .Lft0_old
	s_mov_b32 s12, 0x21500
	v_lshl_add_u32 v130, s62, 6, v239
	v_lshl_add_u32 v131, v130, 2, s12
	v_add_u32_e32 v64, v241, v219
	ds_read_b128 v[98:101], v64 offset:32768
	v_add_u32_e32 v64, v241, v215
	ds_read_b128 v[102:105], v64 offset:32768
	v_add_u32_e32 v64, v241, v186
	ds_read_b128 v[106:109], v64 offset:32768
	v_add_u32_e32 v64, v241, v233
	ds_read_b128 v[110:113], v64 offset:32768
	s_waitcnt lgkmcnt(3)
	v_mfma_f32_32x32x16_bf16 v[82:97], v[98:101], v[144:147], 0
	v_add_u32_e32 v64, v241, v234
	ds_read_b128 v[98:101], v64 offset:32768
	s_waitcnt lgkmcnt(3)
	v_mfma_f32_32x32x16_bf16 v[82:97], v[102:105], v[148:151], v[82:97]
	v_add_u32_e32 v64, v241, v235
	ds_read_b128 v[102:105], v64 offset:32768
	s_waitcnt lgkmcnt(3)
	v_mfma_f32_32x32x16_bf16 v[82:97], v[106:109], v[152:155], v[82:97]
	v_add_u32_e32 v64, v241, v236
	ds_read_b128 v[106:109], v64 offset:32768
	s_waitcnt lgkmcnt(3)
	v_mfma_f32_32x32x16_bf16 v[82:97], v[110:113], v[156:159], v[82:97]
	v_add_u32_e32 v64, v241, v237
	ds_read_b128 v[110:113], v64 offset:32768
	s_waitcnt lgkmcnt(3)
	v_mfma_f32_32x32x16_bf16 v[82:97], v[98:101], v[160:163], v[82:97]
	v_add_u32_e32 v64, v241, v219
	ds_read_b128 v[98:101], v64 offset:40960
	s_waitcnt lgkmcnt(3)
	v_mfma_f32_32x32x16_bf16 v[82:97], v[102:105], v[164:167], v[82:97]
	v_add_u32_e32 v64, v241, v215
	ds_read_b128 v[102:105], v64 offset:40960
	s_waitcnt lgkmcnt(3)
	v_mfma_f32_32x32x16_bf16 v[82:97], v[106:109], v[168:171], v[82:97]
	v_add_u32_e32 v64, v241, v186
	ds_read_b128 v[106:109], v64 offset:40960
	s_waitcnt lgkmcnt(3)
	v_mfma_f32_32x32x16_bf16 v[82:97], v[110:113], v[172:175], v[82:97]
	v_add_u32_e32 v64, v241, v233
	ds_read_b128 v[110:113], v64 offset:40960
	ds_read2_b32 v[114:115], v131 offset0:128 offset1:129
	ds_read2_b32 v[116:117], v131 offset0:130 offset1:131
	ds_read2_b32 v[118:119], v131 offset0:136 offset1:137
	ds_read2_b32 v[120:121], v131 offset0:138 offset1:139
	ds_read2_b32 v[122:123], v131 offset0:144 offset1:145
	ds_read2_b32 v[124:125], v131 offset0:146 offset1:147
	ds_read2_b32 v[126:127], v131 offset0:152 offset1:153
	ds_read2_b32 v[128:129], v131 offset0:154 offset1:155
	s_waitcnt lgkmcnt(11)
	v_mfma_f32_32x32x16_bf16 v[66:81], v[98:101], v[144:147], 0
	v_add_u32_e32 v64, v241, v234
	ds_read_b128 v[98:101], v64 offset:40960
	s_waitcnt lgkmcnt(11)
	v_mfma_f32_32x32x16_bf16 v[66:81], v[102:105], v[148:151], v[66:81]
	v_add_u32_e32 v64, v241, v235
	ds_read_b128 v[102:105], v64 offset:40960
	s_waitcnt lgkmcnt(11)
	v_mfma_f32_32x32x16_bf16 v[66:81], v[106:109], v[152:155], v[66:81]
	v_add_u32_e32 v64, v241, v236
	ds_read_b128 v[106:109], v64 offset:40960
	s_waitcnt lgkmcnt(11)
	v_mfma_f32_32x32x16_bf16 v[66:81], v[110:113], v[156:159], v[66:81]
	v_add_u32_e32 v64, v241, v237
	ds_read_b128 v[110:113], v64 offset:40960
	s_waitcnt lgkmcnt(3)
	v_mfma_f32_32x32x16_bf16 v[66:81], v[98:101], v[160:163], v[66:81]
	s_waitcnt lgkmcnt(2)
	v_mfma_f32_32x32x16_bf16 v[66:81], v[102:105], v[164:167], v[66:81]
	s_waitcnt lgkmcnt(1)
	v_mfma_f32_32x32x16_bf16 v[66:81], v[106:109], v[168:171], v[66:81]
	s_waitcnt lgkmcnt(0)
	v_mfma_f32_32x32x16_bf16 v[66:81], v[110:113], v[172:175], v[66:81]
	v_pk_fma_f32 v[82:83], v[82:83], s[94:95], v[114:115] op_sel_hi:[1,0,1]
	v_pk_fma_f32 v[84:85], v[84:85], s[94:95], v[116:117] op_sel_hi:[1,0,1]
	v_pk_fma_f32 v[86:87], v[86:87], s[94:95], v[118:119] op_sel_hi:[1,0,1]
	v_pk_fma_f32 v[88:89], v[88:89], s[94:95], v[120:121] op_sel_hi:[1,0,1]
	v_pk_fma_f32 v[90:91], v[90:91], s[94:95], v[122:123] op_sel_hi:[1,0,1]
	v_pk_fma_f32 v[92:93], v[92:93], s[94:95], v[124:125] op_sel_hi:[1,0,1]
	v_pk_fma_f32 v[94:95], v[94:95], s[94:95], v[126:127] op_sel_hi:[1,0,1]
	v_pk_fma_f32 v[96:97], v[96:97], s[94:95], v[128:129] op_sel_hi:[1,0,1]
	v_max_f32_e32 v132, v82, v83
	v_max3_f32 v132, v132, v84, v85
	v_max3_f32 v132, v132, v86, v87
	v_max3_f32 v132, v132, v88, v89
	v_max3_f32 v132, v132, v90, v91
	v_max3_f32 v132, v132, v92, v93
	v_max3_f32 v132, v132, v94, v95
	v_max3_f32 v132, v132, v96, v97
	ds_read2_b32 v[114:115], v131 offset0:160 offset1:161
	ds_read2_b32 v[116:117], v131 offset0:162 offset1:163
	ds_read2_b32 v[118:119], v131 offset0:168 offset1:169
	ds_read2_b32 v[120:121], v131 offset0:170 offset1:171
	ds_read2_b32 v[122:123], v131 offset0:176 offset1:177
	ds_read2_b32 v[124:125], v131 offset0:178 offset1:179
	ds_read2_b32 v[126:127], v131 offset0:184 offset1:185
	ds_read2_b32 v[128:129], v131 offset0:186 offset1:187
	ds_read_b64_tr_b16 v[98:99], v240 offset:0
	ds_read_b64_tr_b16 v[100:101], v240 offset:2048
	ds_read_b64_tr_b16 v[102:103], v240 offset:512
	ds_read_b64_tr_b16 v[104:105], v240 offset:2560
	ds_read_b64_tr_b16 v[106:107], v240 offset:4096
	ds_read_b64_tr_b16 v[108:109], v240 offset:6144
	s_waitcnt lgkmcnt(13)
	v_pk_fma_f32 v[66:67], v[66:67], s[94:95], v[114:115] op_sel_hi:[1,0,1]
	s_waitcnt lgkmcnt(12)
	v_pk_fma_f32 v[68:69], v[68:69], s[94:95], v[116:117] op_sel_hi:[1,0,1]
	s_waitcnt lgkmcnt(11)
	v_pk_fma_f32 v[70:71], v[70:71], s[94:95], v[118:119] op_sel_hi:[1,0,1]
	s_waitcnt lgkmcnt(10)
	v_pk_fma_f32 v[72:73], v[72:73], s[94:95], v[120:121] op_sel_hi:[1,0,1]
	s_waitcnt lgkmcnt(9)
	v_pk_fma_f32 v[74:75], v[74:75], s[94:95], v[122:123] op_sel_hi:[1,0,1]
	s_waitcnt lgkmcnt(8)
	v_pk_fma_f32 v[76:77], v[76:77], s[94:95], v[124:125] op_sel_hi:[1,0,1]
	s_waitcnt lgkmcnt(7)
	v_pk_fma_f32 v[78:79], v[78:79], s[94:95], v[126:127] op_sel_hi:[1,0,1]
	s_waitcnt lgkmcnt(6)
	v_pk_fma_f32 v[80:81], v[80:81], s[94:95], v[128:129] op_sel_hi:[1,0,1]
	ds_read_b64_tr_b16 v[110:111], v240 offset:4608
	ds_read_b64_tr_b16 v[112:113], v240 offset:6656
	v_max3_f32 v132, v132, v66, v67
	v_max3_f32 v132, v132, v68, v69
	v_max3_f32 v132, v132, v70, v71
	v_max3_f32 v132, v132, v72, v73
	v_max3_f32 v132, v132, v74, v75
	v_max3_f32 v132, v132, v76, v77
	v_max3_f32 v132, v132, v78, v79
	v_max3_f32 v132, v132, v80, v81
	v_mov_b32_e32 v133, v132
	s_nop 1
	v_permlane32_swap_b32_e32 v132, v133
	v_max3_f32 v243, v245, v132, v133
	v_sub_f32_e32 v134, v243, v245
	v_cmp_lt_f32_e32 vcc, 0x41000000, v134
	s_cbranch_vccnz .Lft0_newmax
	v_mov_b32_e32 v243, v245
; __device__ __forceinline__ int crow(int r, int hi) { return (r & 3) + 8 * (r >> 2) + 4 * hi; }
; __device__ __forceinline__ void datt_stream(LAS unsigned char* lds, const DattRun& c, const float C, const int wv) {
;     ...
;         const float mn = fmaxf(m_reg, pmax), alpha = __builtin_amdgcn_exp2f(m_reg - mn); m_reg = mn;
;         float ps = 0.f;
;         if (do0) {
; #pragma unroll
;             for (int r = 0; r < 16; ++r) { p0[r] = __builtin_amdgcn_exp2f(p0[r] - mn); ps += p0[r]; } }
;         if (do1) {
; #pragma unroll
;             for (int r = 0; r < 16; ++r) { p1[r] = __builtin_amdgcn_exp2f(p1[r] - mn); ps += p1[r]; } }
;         { auto rr = __builtin_amdgcn_permlane32_swap(__float_as_uint(ps), __float_as_uint(ps), false, false);
;           ps = __uint_as_float(rr[0]) + __uint_as_float(rr[1]); }
;         l_reg = l_reg * alpha + ps;
;         if (__any(alpha < 1.f)) { if (hi == 0) al_l[r32] = alpha; asm volatile("s_waitcnt lgkmcnt(0)" ::: "memory");
; #pragma unroll
;             for (int r = 0; r < 16; ++r) { const float a = al_l[crow(r, hi)];
; #pragma unroll
;                 for (int d = 0; d < 4; ++d) o[d][r] *= a; } }
;         const int vb = vb0 + b * SHM_T;
;     ...
;         if (do0) { bf16x8 pa0_, pa1_; DS_PK4(p0, 0, pa0_); DS_PK4(p0, 8, pa1_);
.Lft0_newmax:
	ds_read_b64_tr_b16 v[114:115], v240 offset:1024
	ds_read_b64_tr_b16 v[116:117], v240 offset:3072
	ds_read_b64_tr_b16 v[118:119], v240 offset:1536
	ds_read_b64_tr_b16 v[120:121], v240 offset:3584
	ds_read_b64_tr_b16 v[122:123], v240 offset:5120
	ds_read_b64_tr_b16 v[124:125], v240 offset:7168
	ds_read_b64_tr_b16 v[126:127], v240 offset:5632
	s_waitcnt lgkmcnt(14)
	ds_read_b64_tr_b16 v[128:129], v240 offset:7680
	v_mov_b32_e32 v132, v243
	v_mov_b32_e32 v133, v243
	v_pk_add_f32 v[82:83], v[82:83], v[132:133] neg_lo:[0,1] neg_hi:[0,1]
	v_pk_add_f32 v[84:85], v[84:85], v[132:133] neg_lo:[0,1] neg_hi:[0,1]
	v_pk_add_f32 v[86:87], v[86:87], v[132:133] neg_lo:[0,1] neg_hi:[0,1]
	v_pk_add_f32 v[88:89], v[88:89], v[132:133] neg_lo:[0,1] neg_hi:[0,1]
	v_pk_add_f32 v[90:91], v[90:91], v[132:133] neg_lo:[0,1] neg_hi:[0,1]
	v_pk_add_f32 v[92:93], v[92:93], v[132:133] neg_lo:[0,1] neg_hi:[0,1]
	v_pk_add_f32 v[94:95], v[94:95], v[132:133] neg_lo:[0,1] neg_hi:[0,1]
	v_pk_add_f32 v[96:97], v[96:97], v[132:133] neg_lo:[0,1] neg_hi:[0,1]
	v_exp_f32_e32 v82, v82
	v_exp_f32_e32 v83, v83
	v_exp_f32_e32 v84, v84
	v_exp_f32_e32 v85, v85
	v_exp_f32_e32 v86, v86
	v_exp_f32_e32 v87, v87
	v_exp_f32_e32 v88, v88
	v_exp_f32_e32 v89, v89
	v_exp_f32_e32 v90, v90
	v_exp_f32_e32 v91, v91
	v_exp_f32_e32 v92, v92
	v_exp_f32_e32 v93, v93
	v_exp_f32_e32 v94, v94
	v_exp_f32_e32 v95, v95
	v_exp_f32_e32 v96, v96
	v_exp_f32_e32 v97, v97
	v_pk_add_f32 v[136:137], v[82:83], v[84:85]
	v_pk_add_f32 v[136:137], v[136:137], v[86:87]
	v_pk_add_f32 v[136:137], v[136:137], v[88:89]
	v_pk_add_f32 v[136:137], v[136:137], v[90:91]
	v_pk_add_f32 v[136:137], v[136:137], v[92:93]
	v_pk_add_f32 v[136:137], v[136:137], v[94:95]
	v_pk_add_f32 v[136:137], v[136:137], v[96:97]
	v_sub_f32_e32 v134, v245, v243
	v_exp_f32_e32 v245, v134
	v_cvt_pk_bf16_f32 v82, v82, v83
	v_cvt_pk_bf16_f32 v83, v84, v85
	v_cvt_pk_bf16_f32 v84, v86, v87
	v_cvt_pk_bf16_f32 v85, v88, v89
	v_cvt_pk_bf16_f32 v86, v90, v91
	v_cvt_pk_bf16_f32 v87, v92, v93
	v_cvt_pk_bf16_f32 v88, v94, v95
	v_cvt_pk_bf16_f32 v89, v96, v97
	s_cmp_eq_u32 s62, 0
	s_cbranch_scc1 .Lft0_noresc
	v_cmp_gt_f32_e32 vcc, 1.0, v245
	s_cbranch_vccz .Lft0_noresc
	s_and_saveexec_b64 s[0:1], s[4:5]
	ds_write_b32 v229, v245 offset:128
	s_or_b64 exec, exec, s[0:1]
	s_waitcnt lgkmcnt(0)
	v_add_u32_e32 v134, s60, v230
	ds_read_b128 v[114:117], v134 offset:128
	ds_read_b128 v[118:121], v134 offset:160
	ds_read_b128 v[122:125], v134 offset:192
	ds_read_b128 v[126:129], v134 offset:224
	s_waitcnt lgkmcnt(0)
	v_pk_mul_f32 v[0:1], v[0:1], v[114:115]
	v_pk_mul_f32 v[2:3], v[2:3], v[116:117]
	v_pk_mul_f32 v[4:5], v[4:5], v[118:119]
	v_pk_mul_f32 v[6:7], v[6:7], v[120:121]
	v_pk_mul_f32 v[8:9], v[8:9], v[122:123]
	v_pk_mul_f32 v[10:11], v[10:11], v[124:125]
	v_pk_mul_f32 v[12:13], v[12:13], v[126:127]
	v_pk_mul_f32 v[14:15], v[14:15], v[128:129]
	v_pk_mul_f32 v[16:17], v[16:17], v[114:115]
	v_pk_mul_f32 v[18:19], v[18:19], v[116:117]
	v_pk_mul_f32 v[20:21], v[20:21], v[118:119]
	v_pk_mul_f32 v[22:23], v[22:23], v[120:121]
	v_pk_mul_f32 v[24:25], v[24:25], v[122:123]
	v_pk_mul_f32 v[26:27], v[26:27], v[124:125]
	v_pk_mul_f32 v[28:29], v[28:29], v[126:127]
	v_pk_mul_f32 v[30:31], v[30:31], v[128:129]
	v_pk_mul_f32 v[32:33], v[32:33], v[114:115]
	v_pk_mul_f32 v[34:35], v[34:35], v[116:117]
	v_pk_mul_f32 v[36:37], v[36:37], v[118:119]
	v_pk_mul_f32 v[38:39], v[38:39], v[120:121]
	v_pk_mul_f32 v[40:41], v[40:41], v[122:123]
	v_pk_mul_f32 v[42:43], v[42:43], v[124:125]
	v_pk_mul_f32 v[44:45], v[44:45], v[126:127]
	v_pk_mul_f32 v[46:47], v[46:47], v[128:129]
	v_pk_mul_f32 v[48:49], v[48:49], v[114:115]
	v_pk_mul_f32 v[50:51], v[50:51], v[116:117]
	v_pk_mul_f32 v[52:53], v[52:53], v[118:119]
	v_pk_mul_f32 v[54:55], v[54:55], v[120:121]
	v_pk_mul_f32 v[56:57], v[56:57], v[122:123]
	v_pk_mul_f32 v[58:59], v[58:59], v[124:125]
	v_pk_mul_f32 v[60:61], v[60:61], v[126:127]
	v_pk_mul_f32 v[62:63], v[62:63], v[128:129]
	ds_read_b64_tr_b16 v[114:115], v240 offset:1024
	ds_read_b64_tr_b16 v[116:117], v240 offset:3072
	ds_read_b64_tr_b16 v[118:119], v240 offset:1536
	ds_read_b64_tr_b16 v[120:121], v240 offset:3584
	ds_read_b64_tr_b16 v[122:123], v240 offset:5120
	ds_read_b64_tr_b16 v[124:125], v240 offset:7168
	ds_read_b64_tr_b16 v[126:127], v240 offset:5632
	ds_read_b64_tr_b16 v[128:129], v240 offset:7680
	s_nop 1
; __device__ __forceinline__ int crow(int r, int hi) { return (r & 3) + 8 * (r >> 2) + 4 * hi; }
; __device__ __forceinline__ void datt_stream(LAS unsigned char* lds, const DattRun& c, const float C, const int wv) {
;     ...
;             for (int r = 0; r < 16; ++r) { p0[r] = __builtin_amdgcn_exp2f(p0[r] - mn); ps += p0[r]; } }
;         if (do1) {
; #pragma unroll
;             for (int r = 0; r < 16; ++r) { p1[r] = __builtin_amdgcn_exp2f(p1[r] - mn); ps += p1[r]; } }
;         { auto rr = __builtin_amdgcn_permlane32_swap(__float_as_uint(ps), __float_as_uint(ps), false, false);
;           ps = __uint_as_float(rr[0]) + __uint_as_float(rr[1]); }
;         l_reg = l_reg * alpha + ps;
;         if (__any(alpha < 1.f)) { if (hi == 0) al_l[r32] = alpha; asm volatile("s_waitcnt lgkmcnt(0)" ::: "memory");
; #pragma unroll
;             for (int r = 0; r < 16; ++r) { const float a = al_l[crow(r, hi)];
; #pragma unroll
;                 for (int d = 0; d < 4; ++d) o[d][r] *= a; } }
;         const int vb = vb0 + b * SHM_T;
;     ...
;         if (do0) { bf16x8 pa0_, pa1_; DS_PK4(p0, 0, pa0_); DS_PK4(p0, 8, pa1_);
;             pv_half2<0, 1, 0>(o[0], o[1], vb, pa0_, pa1_); pv_half2<2, 3, 0>(o[2], o[3], vb, pa0_, pa1_); }
;         if (do1) { bf16x8 pa2_, pa3_; DS_PK4(p1, 0, pa2_); DS_PK4(p1, 8, pa3_);
;             pv_half2<0, 1, 1>(o[0], o[1], vb, pa2_, pa3_); pv_half2<2, 3, 1>(o[2], o[3], vb, pa2_, pa3_); }
.Lft0_noresc:
	v_permlane32_swap_b32_e32 v82, v84
	v_permlane32_swap_b32_e32 v83, v85
	v_permlane32_swap_b32_e32 v86, v88
	v_permlane32_swap_b32_e32 v87, v89
	v_pk_add_f32 v[66:67], v[66:67], v[132:133] neg_lo:[0,1] neg_hi:[0,1]
	v_pk_add_f32 v[68:69], v[68:69], v[132:133] neg_lo:[0,1] neg_hi:[0,1]
	v_pk_add_f32 v[70:71], v[70:71], v[132:133] neg_lo:[0,1] neg_hi:[0,1]
	v_pk_add_f32 v[72:73], v[72:73], v[132:133] neg_lo:[0,1] neg_hi:[0,1]
	v_pk_add_f32 v[74:75], v[74:75], v[132:133] neg_lo:[0,1] neg_hi:[0,1]
	v_pk_add_f32 v[76:77], v[76:77], v[132:133] neg_lo:[0,1] neg_hi:[0,1]
	v_pk_add_f32 v[78:79], v[78:79], v[132:133] neg_lo:[0,1] neg_hi:[0,1]
	v_pk_add_f32 v[80:81], v[80:81], v[132:133] neg_lo:[0,1] neg_hi:[0,1]
	v_exp_f32_e32 v66, v66
	v_exp_f32_e32 v67, v67
	v_exp_f32_e32 v68, v68
	v_exp_f32_e32 v69, v69
	v_exp_f32_e32 v70, v70
	v_exp_f32_e32 v71, v71
	v_exp_f32_e32 v72, v72
	v_exp_f32_e32 v73, v73
	v_exp_f32_e32 v74, v74
	v_exp_f32_e32 v75, v75
	v_exp_f32_e32 v76, v76
	v_exp_f32_e32 v77, v77
	v_exp_f32_e32 v78, v78
	v_exp_f32_e32 v79, v79
	v_exp_f32_e32 v80, v80
	v_exp_f32_e32 v81, v81
	v_pk_add_f32 v[136:137], v[136:137], v[66:67]
	v_pk_add_f32 v[136:137], v[136:137], v[68:69]
	v_pk_add_f32 v[136:137], v[136:137], v[70:71]
	v_pk_add_f32 v[136:137], v[136:137], v[72:73]
	v_pk_add_f32 v[136:137], v[136:137], v[74:75]
	v_pk_add_f32 v[136:137], v[136:137], v[76:77]
	v_pk_add_f32 v[136:137], v[136:137], v[78:79]
	v_pk_add_f32 v[136:137], v[136:137], v[80:81]
	v_add_f32_e32 v64, v136, v137
	s_waitcnt lgkmcnt(14)
	v_mfma_f32_32x32x16_bf16 v[0:15], v[82:85], v[98:101], v[0:15]
	ds_read_b64_tr_b16 v[98:99], v240 offset:8192
	s_waitcnt lgkmcnt(14)
	ds_read_b64_tr_b16 v[100:101], v240 offset:10240
	s_waitcnt lgkmcnt(14)
	v_mfma_f32_32x32x16_bf16 v[16:31], v[82:85], v[102:105], v[16:31]
	ds_read_b64_tr_b16 v[102:103], v240 offset:8704
	s_waitcnt lgkmcnt(14)
	ds_read_b64_tr_b16 v[104:105], v240 offset:10752
	s_waitcnt lgkmcnt(14)
	v_mfma_f32_32x32x16_bf16 v[0:15], v[86:89], v[106:109], v[0:15]
	ds_read_b64_tr_b16 v[106:107], v240 offset:12288
	s_waitcnt lgkmcnt(14)
	ds_read_b64_tr_b16 v[108:109], v240 offset:14336
	s_waitcnt lgkmcnt(14)
	v_mfma_f32_32x32x16_bf16 v[16:31], v[86:89], v[110:113], v[16:31]
	ds_read_b64_tr_b16 v[110:111], v240 offset:12800
	s_waitcnt lgkmcnt(14)
	ds_read_b64_tr_b16 v[112:113], v240 offset:14848
	s_waitcnt lgkmcnt(14)
	v_mfma_f32_32x32x16_bf16 v[32:47], v[82:85], v[114:117], v[32:47]
	ds_read_b64_tr_b16 v[114:115], v240 offset:9216
	s_waitcnt lgkmcnt(14)
	ds_read_b64_tr_b16 v[116:117], v240 offset:11264
	s_waitcnt lgkmcnt(14)
	v_mfma_f32_32x32x16_bf16 v[48:63], v[82:85], v[118:121], v[48:63]
	ds_read_b64_tr_b16 v[118:119], v240 offset:9728
	s_waitcnt lgkmcnt(14)
	ds_read_b64_tr_b16 v[120:121], v240 offset:11776
	s_waitcnt lgkmcnt(14)
	v_mfma_f32_32x32x16_bf16 v[32:47], v[86:89], v[122:125], v[32:47]
	ds_read_b64_tr_b16 v[122:123], v240 offset:13312
	s_waitcnt lgkmcnt(14)
	ds_read_b64_tr_b16 v[124:125], v240 offset:15360
	s_waitcnt lgkmcnt(14)
	v_mfma_f32_32x32x16_bf16 v[48:63], v[86:89], v[126:129], v[48:63]
	ds_read_b64_tr_b16 v[126:127], v240 offset:13824
	s_waitcnt lgkmcnt(14)
	ds_read_b64_tr_b16 v[128:129], v240 offset:15872
	v_cvt_pk_bf16_f32 v66, v66, v67
	v_cvt_pk_bf16_f32 v67, v68, v69
	v_cvt_pk_bf16_f32 v68, v70, v71
	v_cvt_pk_bf16_f32 v69, v72, v73
	v_cvt_pk_bf16_f32 v70, v74, v75
	v_cvt_pk_bf16_f32 v71, v76, v77
	v_cvt_pk_bf16_f32 v72, v78, v79
	v_cvt_pk_bf16_f32 v73, v80, v81
	v_mov_b32_e32 v244, v64
	v_permlane32_swap_b32_e32 v66, v68
	v_permlane32_swap_b32_e32 v67, v69
	v_permlane32_swap_b32_e32 v70, v72
	v_permlane32_swap_b32_e32 v71, v73
	v_permlane32_swap_b32_e32 v64, v244
	s_waitcnt lgkmcnt(14)
	v_mfma_f32_32x32x16_bf16 v[0:15], v[66:69], v[98:101], v[0:15]
	s_waitcnt lgkmcnt(12)
	v_mfma_f32_32x32x16_bf16 v[16:31], v[66:69], v[102:105], v[16:31]
	s_waitcnt lgkmcnt(10)
	v_mfma_f32_32x32x16_bf16 v[0:15], v[70:73], v[106:109], v[0:15]
	s_waitcnt lgkmcnt(8)
	v_mfma_f32_32x32x16_bf16 v[16:31], v[70:73], v[110:113], v[16:31]
	s_waitcnt lgkmcnt(6)
	v_mfma_f32_32x32x16_bf16 v[32:47], v[66:69], v[114:117], v[32:47]
	s_waitcnt lgkmcnt(4)
	v_mfma_f32_32x32x16_bf16 v[48:63], v[66:69], v[118:121], v[48:63]
	s_waitcnt lgkmcnt(2)
	v_mfma_f32_32x32x16_bf16 v[32:47], v[70:73], v[122:125], v[32:47]
	s_waitcnt lgkmcnt(0)
	v_mfma_f32_32x32x16_bf16 v[48:63], v[70:73], v[126:129], v[48:63]
	s_nop 1
	s_branch .LBB0_463

; #define LAS __attribute__((address_space(3)))
; __device__ __forceinline__ void datt_stream(LAS unsigned char* lds, const DattRun& c, const float C, const int wv) {
;     ...
;         if (do0) {
; #pragma unroll
;             for (int d0 = 0; d0 < 8; ++d0) { const bf16x8 b0 = *(const LAS bf16x8*)(Ks + ATT_KSWZ(r32, (d0 * 16 + hi * 8) * 2)); p0 = __builtin_amdgcn_mfma_f32_32x32x16_bf16(b0, qr[d0], p0, 0, 0, 0); } }
;         if (do1) {
; #pragma unroll
;             for (int d0 = 0; d0 < 8; ++d0) { const bf16x8 b1 = *(const LAS bf16x8*)(Ks + ATT_KSWZ(32 + r32, (d0 * 16 + hi * 8) * 2)); p1 = __builtin_amdgcn_mfma_f32_32x32x16_bf16(b1, qr[d0], p1, 0, 0, 0); } }
;         const int db = 64 * (rel - 1) - 32 * par - r32 + 4 * hi, qi = 64 * (c.a0 + pa) + 32 * par + r32; const unsigned L = (unsigned)c.L;
;         const LAS float* tb = c.tb + (db + 2 * HALFWIN);
;     ...
;         if (do0) DS_XFORM(p0, 0);
;         if (do1) DS_XFORM(p1, 32);
;     ...
;         float pmax = -__builtin_inff();
;         if (do0) {
; #pragma unroll
;             for (int r = 0; r < 16; ++r) pmax = fmaxf(pmax, p0[r]); }
;         if (do1) {
; #pragma unroll
;             for (int r = 0; r < 16; ++r) pmax = fmaxf(pmax, p1[r]); }
;         { auto rr = __builtin_amdgcn_permlane32_swap(__float_as_uint(pmax), __float_as_uint(pmax), false, false);
;           pmax = fmaxf(__uint_as_float(rr[0]), __uint_as_float(rr[1])); }
;         const float mn = fmaxf(m_reg, pmax), alpha = __builtin_amdgcn_exp2f(m_reg - mn); m_reg = mn;
.LBB0_485:
	s_cmp_lg_u32 s12, 2
	s_cselect_b64 s[8:9], -1, 0
	s_cmp_eq_u32 s12, 2
	v_add_u32_e32 v0, v241, v219
	v_add_u32_e32 v38, v241, v215
	v_add_u32_e32 v37, v241, v186
	v_add_u32_e32 v36, v241, v233
	v_add_u32_e32 v35, v241, v234
	v_add_u32_e32 v34, v241, v235
	v_add_u32_e32 v33, v241, v236
	v_add_u32_e32 v32, v241, v237
	s_cbranch_scc1 .LBB0_489
	s_cmp_eq_u32 s12, 3
	s_cbranch_scc1 .Lft1_old
	s_cmp_lg_u64 s[10:11], 0
	s_cbranch_scc1 .Lft1_old
	s_mov_b32 s12, 0x21500
	v_lshl_add_u32 v69, s63, 6, v239
	v_lshl_add_u32 v68, v69, 2, s12
	v_add_u32_e32 v64, v241, v219
	ds_read_b128 v[32:35], v64 offset:49152
	v_add_u32_e32 v64, v241, v215
	ds_read_b128 v[36:39], v64 offset:49152
	v_add_u32_e32 v64, v241, v186
	ds_read_b128 v[40:43], v64 offset:49152
	v_add_u32_e32 v64, v241, v233
	ds_read_b128 v[44:47], v64 offset:49152
	s_waitcnt lgkmcnt(3)
	v_mfma_f32_32x32x16_bf16 v[16:31], v[32:35], v[144:147], 0
	v_add_u32_e32 v64, v241, v234
	ds_read_b128 v[32:35], v64 offset:49152
	s_waitcnt lgkmcnt(3)
	v_mfma_f32_32x32x16_bf16 v[16:31], v[36:39], v[148:151], v[16:31]
	v_add_u32_e32 v64, v241, v235
	ds_read_b128 v[36:39], v64 offset:49152
	s_waitcnt lgkmcnt(3)
	v_mfma_f32_32x32x16_bf16 v[16:31], v[40:43], v[152:155], v[16:31]
	v_add_u32_e32 v64, v241, v236
	ds_read_b128 v[40:43], v64 offset:49152
	s_waitcnt lgkmcnt(3)
	v_mfma_f32_32x32x16_bf16 v[16:31], v[44:47], v[156:159], v[16:31]
	v_add_u32_e32 v64, v241, v237
	ds_read_b128 v[44:47], v64 offset:49152
	s_waitcnt lgkmcnt(3)
	v_mfma_f32_32x32x16_bf16 v[16:31], v[32:35], v[160:163], v[16:31]
	v_add_u32_e32 v64, v241, v219
	ds_read_b128 v[32:35], v64 offset:57344
	s_waitcnt lgkmcnt(3)
	v_mfma_f32_32x32x16_bf16 v[16:31], v[36:39], v[164:167], v[16:31]
	v_add_u32_e32 v64, v241, v215
	ds_read_b128 v[36:39], v64 offset:57344
	s_waitcnt lgkmcnt(3)
	v_mfma_f32_32x32x16_bf16 v[16:31], v[40:43], v[168:171], v[16:31]
	v_add_u32_e32 v64, v241, v186
	ds_read_b128 v[40:43], v64 offset:57344
	s_waitcnt lgkmcnt(3)
	v_mfma_f32_32x32x16_bf16 v[16:31], v[44:47], v[172:175], v[16:31]
	v_add_u32_e32 v64, v241, v233
	ds_read_b128 v[44:47], v64 offset:57344
	ds_read2_b32 v[48:49], v68 offset0:128 offset1:129
	ds_read2_b32 v[50:51], v68 offset0:130 offset1:131
	ds_read2_b32 v[52:53], v68 offset0:136 offset1:137
	ds_read2_b32 v[54:55], v68 offset0:138 offset1:139
	ds_read2_b32 v[56:57], v68 offset0:144 offset1:145
	ds_read2_b32 v[58:59], v68 offset0:146 offset1:147
	ds_read2_b32 v[60:61], v68 offset0:152 offset1:153
	ds_read2_b32 v[62:63], v68 offset0:154 offset1:155
	s_waitcnt lgkmcnt(11)
	v_mfma_f32_32x32x16_bf16 v[0:15], v[32:35], v[144:147], 0
	v_add_u32_e32 v64, v241, v234
	ds_read_b128 v[32:35], v64 offset:57344
	s_waitcnt lgkmcnt(11)
	v_mfma_f32_32x32x16_bf16 v[0:15], v[36:39], v[148:151], v[0:15]
	v_add_u32_e32 v64, v241, v235
	ds_read_b128 v[36:39], v64 offset:57344
	s_waitcnt lgkmcnt(11)
	v_mfma_f32_32x32x16_bf16 v[0:15], v[40:43], v[152:155], v[0:15]
	v_add_u32_e32 v64, v241, v236
	ds_read_b128 v[40:43], v64 offset:57344
	s_waitcnt lgkmcnt(11)
	v_mfma_f32_32x32x16_bf16 v[0:15], v[44:47], v[156:159], v[0:15]
	v_add_u32_e32 v64, v241, v237
	ds_read_b128 v[44:47], v64 offset:57344
	s_waitcnt lgkmcnt(3)
	v_mfma_f32_32x32x16_bf16 v[0:15], v[32:35], v[160:163], v[0:15]
	s_waitcnt lgkmcnt(2)
	v_mfma_f32_32x32x16_bf16 v[0:15], v[36:39], v[164:167], v[0:15]
	s_waitcnt lgkmcnt(1)
	v_mfma_f32_32x32x16_bf16 v[0:15], v[40:43], v[168:171], v[0:15]
	s_waitcnt lgkmcnt(0)
	v_mfma_f32_32x32x16_bf16 v[0:15], v[44:47], v[172:175], v[0:15]
	v_pk_fma_f32 v[16:17], v[16:17], s[94:95], v[48:49] op_sel_hi:[1,0,1]
	v_pk_fma_f32 v[18:19], v[18:19], s[94:95], v[50:51] op_sel_hi:[1,0,1]
	v_pk_fma_f32 v[20:21], v[20:21], s[94:95], v[52:53] op_sel_hi:[1,0,1]
	v_pk_fma_f32 v[22:23], v[22:23], s[94:95], v[54:55] op_sel_hi:[1,0,1]
	v_pk_fma_f32 v[24:25], v[24:25], s[94:95], v[56:57] op_sel_hi:[1,0,1]
	v_pk_fma_f32 v[26:27], v[26:27], s[94:95], v[58:59] op_sel_hi:[1,0,1]
	v_pk_fma_f32 v[28:29], v[28:29], s[94:95], v[60:61] op_sel_hi:[1,0,1]
	v_pk_fma_f32 v[30:31], v[30:31], s[94:95], v[62:63] op_sel_hi:[1,0,1]
	v_max_f32_e32 v70, v16, v17
	v_max3_f32 v70, v70, v18, v19
	v_max3_f32 v70, v70, v20, v21
	v_max3_f32 v70, v70, v22, v23
	v_max3_f32 v70, v70, v24, v25
	v_max3_f32 v70, v70, v26, v27
	v_max3_f32 v70, v70, v28, v29
	v_max3_f32 v70, v70, v30, v31
	ds_read2_b32 v[48:49], v68 offset0:160 offset1:161
	ds_read2_b32 v[50:51], v68 offset0:162 offset1:163
	ds_read2_b32 v[52:53], v68 offset0:168 offset1:169
	ds_read2_b32 v[54:55], v68 offset0:170 offset1:171
	ds_read2_b32 v[56:57], v68 offset0:176 offset1:177
	ds_read2_b32 v[58:59], v68 offset0:178 offset1:179
	ds_read2_b32 v[60:61], v68 offset0:184 offset1:185
	ds_read2_b32 v[62:63], v68 offset0:186 offset1:187
	ds_read_b64_tr_b16 v[32:33], v242 offset:0
	ds_read_b64_tr_b16 v[34:35], v242 offset:2048
	ds_read_b64_tr_b16 v[36:37], v242 offset:512
	ds_read_b64_tr_b16 v[38:39], v242 offset:2560
	ds_read_b64_tr_b16 v[40:41], v242 offset:4096
	ds_read_b64_tr_b16 v[42:43], v242 offset:6144
	s_waitcnt lgkmcnt(13)
	v_pk_fma_f32 v[0:1], v[0:1], s[94:95], v[48:49] op_sel_hi:[1,0,1]
	s_waitcnt lgkmcnt(12)
	v_pk_fma_f32 v[2:3], v[2:3], s[94:95], v[50:51] op_sel_hi:[1,0,1]
	s_waitcnt lgkmcnt(11)
	v_pk_fma_f32 v[4:5], v[4:5], s[94:95], v[52:53] op_sel_hi:[1,0,1]
	s_waitcnt lgkmcnt(10)
	v_pk_fma_f32 v[6:7], v[6:7], s[94:95], v[54:55] op_sel_hi:[1,0,1]
	s_waitcnt lgkmcnt(9)
	v_pk_fma_f32 v[8:9], v[8:9], s[94:95], v[56:57] op_sel_hi:[1,0,1]
	s_waitcnt lgkmcnt(8)
	v_pk_fma_f32 v[10:11], v[10:11], s[94:95], v[58:59] op_sel_hi:[1,0,1]
	s_waitcnt lgkmcnt(7)
	v_pk_fma_f32 v[12:13], v[12:13], s[94:95], v[60:61] op_sel_hi:[1,0,1]
	s_waitcnt lgkmcnt(6)
	v_pk_fma_f32 v[14:15], v[14:15], s[94:95], v[62:63] op_sel_hi:[1,0,1]
	ds_read_b64_tr_b16 v[44:45], v242 offset:4608
	ds_read_b64_tr_b16 v[46:47], v242 offset:6656
	v_max3_f32 v70, v70, v0, v1
	v_max3_f32 v70, v70, v2, v3
	v_max3_f32 v70, v70, v4, v5
	v_max3_f32 v70, v70, v6, v7
	v_max3_f32 v70, v70, v8, v9
	v_max3_f32 v70, v70, v10, v11
	v_max3_f32 v70, v70, v12, v13
	v_max3_f32 v70, v70, v14, v15
	v_mov_b32_e32 v71, v70
	s_nop 1
	v_permlane32_swap_b32_e32 v70, v71
	v_max3_f32 v245, v243, v70, v71
	v_sub_f32_e32 v72, v245, v243
	v_cmp_lt_f32_e32 vcc, 0x41000000, v72
	s_cbranch_vccnz .Lft1_newmax
	v_mov_b32_e32 v245, v243
; __device__ __forceinline__ int crow(int r, int hi) { return (r & 3) + 8 * (r >> 2) + 4 * hi; }
; __device__ __forceinline__ void datt_stream(LAS unsigned char* lds, const DattRun& c, const float C, const int wv) {
;     ...
;         const float mn = fmaxf(m_reg, pmax), alpha = __builtin_amdgcn_exp2f(m_reg - mn); m_reg = mn;
;         float ps = 0.f;
;         if (do0) {
; #pragma unroll
;             for (int r = 0; r < 16; ++r) { p0[r] = __builtin_amdgcn_exp2f(p0[r] - mn); ps += p0[r]; } }
;         if (do1) {
; #pragma unroll
;             for (int r = 0; r < 16; ++r) { p1[r] = __builtin_amdgcn_exp2f(p1[r] - mn); ps += p1[r]; } }
;         { auto rr = __builtin_amdgcn_permlane32_swap(__float_as_uint(ps), __float_as_uint(ps), false, false);
;           ps = __uint_as_float(rr[0]) + __uint_as_float(rr[1]); }
;         l_reg = l_reg * alpha + ps;
;         if (__any(alpha < 1.f)) { if (hi == 0) al_l[r32] = alpha; asm volatile("s_waitcnt lgkmcnt(0)" ::: "memory");
; #pragma unroll
;             for (int r = 0; r < 16; ++r) { const float a = al_l[crow(r, hi)];
; #pragma unroll
;                 for (int d = 0; d < 4; ++d) o[d][r] *= a; } }
;         const int vb = vb0 + b * SHM_T;
;     ...
;         if (do0) { bf16x8 pa0_, pa1_; DS_PK4(p0, 0, pa0_); DS_PK4(p0, 8, pa1_);
.Lft1_newmax:
	ds_read_b64_tr_b16 v[48:49], v242 offset:1024
	ds_read_b64_tr_b16 v[50:51], v242 offset:3072
	ds_read_b64_tr_b16 v[52:53], v242 offset:1536
	ds_read_b64_tr_b16 v[54:55], v242 offset:3584
	ds_read_b64_tr_b16 v[56:57], v242 offset:5120
	ds_read_b64_tr_b16 v[58:59], v242 offset:7168
	ds_read_b64_tr_b16 v[60:61], v242 offset:5632
	s_waitcnt lgkmcnt(14)
	ds_read_b64_tr_b16 v[62:63], v242 offset:7680
	v_mov_b32_e32 v70, v245
	v_mov_b32_e32 v71, v245
	v_pk_add_f32 v[16:17], v[16:17], v[70:71] neg_lo:[0,1] neg_hi:[0,1]
	v_pk_add_f32 v[18:19], v[18:19], v[70:71] neg_lo:[0,1] neg_hi:[0,1]
	v_pk_add_f32 v[20:21], v[20:21], v[70:71] neg_lo:[0,1] neg_hi:[0,1]
	v_pk_add_f32 v[22:23], v[22:23], v[70:71] neg_lo:[0,1] neg_hi:[0,1]
	v_pk_add_f32 v[24:25], v[24:25], v[70:71] neg_lo:[0,1] neg_hi:[0,1]
	v_pk_add_f32 v[26:27], v[26:27], v[70:71] neg_lo:[0,1] neg_hi:[0,1]
	v_pk_add_f32 v[28:29], v[28:29], v[70:71] neg_lo:[0,1] neg_hi:[0,1]
	v_pk_add_f32 v[30:31], v[30:31], v[70:71] neg_lo:[0,1] neg_hi:[0,1]
	v_exp_f32_e32 v16, v16
	v_exp_f32_e32 v17, v17
	v_exp_f32_e32 v18, v18
	v_exp_f32_e32 v19, v19
	v_exp_f32_e32 v20, v20
	v_exp_f32_e32 v21, v21
	v_exp_f32_e32 v22, v22
	v_exp_f32_e32 v23, v23
	v_exp_f32_e32 v24, v24
	v_exp_f32_e32 v25, v25
	v_exp_f32_e32 v26, v26
	v_exp_f32_e32 v27, v27
	v_exp_f32_e32 v28, v28
	v_exp_f32_e32 v29, v29
	v_exp_f32_e32 v30, v30
	v_exp_f32_e32 v31, v31
	v_pk_add_f32 v[74:75], v[16:17], v[18:19]
	v_pk_add_f32 v[74:75], v[74:75], v[20:21]
	v_pk_add_f32 v[74:75], v[74:75], v[22:23]
	v_pk_add_f32 v[74:75], v[74:75], v[24:25]
	v_pk_add_f32 v[74:75], v[74:75], v[26:27]
	v_pk_add_f32 v[74:75], v[74:75], v[28:29]
	v_pk_add_f32 v[74:75], v[74:75], v[30:31]
	v_sub_f32_e32 v72, v243, v245
	v_exp_f32_e32 v66, v72
	v_cvt_pk_bf16_f32 v16, v16, v17
	v_cvt_pk_bf16_f32 v17, v18, v19
	v_cvt_pk_bf16_f32 v18, v20, v21
	v_cvt_pk_bf16_f32 v19, v22, v23
	v_cvt_pk_bf16_f32 v20, v24, v25
	v_cvt_pk_bf16_f32 v21, v26, v27
	v_cvt_pk_bf16_f32 v22, v28, v29
	v_cvt_pk_bf16_f32 v23, v30, v31
	s_cmp_eq_u32 s63, 0
	s_cbranch_scc1 .Lft1_noresc
	v_cmp_gt_f32_e32 vcc, 1.0, v66
	s_cbranch_vccz .Lft1_noresc
	s_and_saveexec_b64 s[10:11], s[4:5]
	ds_write_b32 v229, v66 offset:128
	s_or_b64 exec, exec, s[10:11]
	s_waitcnt lgkmcnt(0)
	v_add_u32_e32 v72, s60, v230
	ds_read_b128 v[48:51], v72 offset:128
	ds_read_b128 v[52:55], v72 offset:160
	ds_read_b128 v[56:59], v72 offset:192
	ds_read_b128 v[60:63], v72 offset:224
	s_waitcnt lgkmcnt(0)
	v_pk_mul_f32 v[80:81], v[80:81], v[48:49]
	v_pk_mul_f32 v[82:83], v[82:83], v[50:51]
	v_pk_mul_f32 v[84:85], v[84:85], v[52:53]
	v_pk_mul_f32 v[86:87], v[86:87], v[54:55]
	v_pk_mul_f32 v[88:89], v[88:89], v[56:57]
	v_pk_mul_f32 v[90:91], v[90:91], v[58:59]
	v_pk_mul_f32 v[92:93], v[92:93], v[60:61]
	v_pk_mul_f32 v[94:95], v[94:95], v[62:63]
	v_pk_mul_f32 v[96:97], v[96:97], v[48:49]
	v_pk_mul_f32 v[98:99], v[98:99], v[50:51]
	v_pk_mul_f32 v[100:101], v[100:101], v[52:53]
	v_pk_mul_f32 v[102:103], v[102:103], v[54:55]
	v_pk_mul_f32 v[104:105], v[104:105], v[56:57]
	v_pk_mul_f32 v[106:107], v[106:107], v[58:59]
	v_pk_mul_f32 v[108:109], v[108:109], v[60:61]
	v_pk_mul_f32 v[110:111], v[110:111], v[62:63]
	v_pk_mul_f32 v[112:113], v[112:113], v[48:49]
	v_pk_mul_f32 v[114:115], v[114:115], v[50:51]
	v_pk_mul_f32 v[116:117], v[116:117], v[52:53]
	v_pk_mul_f32 v[118:119], v[118:119], v[54:55]
	v_pk_mul_f32 v[120:121], v[120:121], v[56:57]
	v_pk_mul_f32 v[122:123], v[122:123], v[58:59]
	v_pk_mul_f32 v[124:125], v[124:125], v[60:61]
	v_pk_mul_f32 v[126:127], v[126:127], v[62:63]
	v_pk_mul_f32 v[128:129], v[128:129], v[48:49]
	v_pk_mul_f32 v[130:131], v[130:131], v[50:51]
	v_pk_mul_f32 v[132:133], v[132:133], v[52:53]
	v_pk_mul_f32 v[134:135], v[134:135], v[54:55]
	v_pk_mul_f32 v[136:137], v[136:137], v[56:57]
	v_pk_mul_f32 v[138:139], v[138:139], v[58:59]
	v_pk_mul_f32 v[140:141], v[140:141], v[60:61]
	v_pk_mul_f32 v[142:143], v[142:143], v[62:63]
	ds_read_b64_tr_b16 v[48:49], v242 offset:1024
	ds_read_b64_tr_b16 v[50:51], v242 offset:3072
	ds_read_b64_tr_b16 v[52:53], v242 offset:1536
	ds_read_b64_tr_b16 v[54:55], v242 offset:3584
	ds_read_b64_tr_b16 v[56:57], v242 offset:5120
	ds_read_b64_tr_b16 v[58:59], v242 offset:7168
	ds_read_b64_tr_b16 v[60:61], v242 offset:5632
	ds_read_b64_tr_b16 v[62:63], v242 offset:7680
	s_nop 1
; __device__ __forceinline__ int crow(int r, int hi) { return (r & 3) + 8 * (r >> 2) + 4 * hi; }
; __device__ __forceinline__ void datt_stream(LAS unsigned char* lds, const DattRun& c, const float C, const int wv) {
;     ...
;             for (int r = 0; r < 16; ++r) { p0[r] = __builtin_amdgcn_exp2f(p0[r] - mn); ps += p0[r]; } }
;         if (do1) {
; #pragma unroll
;             for (int r = 0; r < 16; ++r) { p1[r] = __builtin_amdgcn_exp2f(p1[r] - mn); ps += p1[r]; } }
;         { auto rr = __builtin_amdgcn_permlane32_swap(__float_as_uint(ps), __float_as_uint(ps), false, false);
;           ps = __uint_as_float(rr[0]) + __uint_as_float(rr[1]); }
;         l_reg = l_reg * alpha + ps;
;         if (__any(alpha < 1.f)) { if (hi == 0) al_l[r32] = alpha; asm volatile("s_waitcnt lgkmcnt(0)" ::: "memory");
; #pragma unroll
;             for (int r = 0; r < 16; ++r) { const float a = al_l[crow(r, hi)];
; #pragma unroll
;                 for (int d = 0; d < 4; ++d) o[d][r] *= a; } }
;         const int vb = vb0 + b * SHM_T;
;     ...
;         if (do0) { bf16x8 pa0_, pa1_; DS_PK4(p0, 0, pa0_); DS_PK4(p0, 8, pa1_);
;             pv_half2<0, 1, 0>(o[0], o[1], vb, pa0_, pa1_); pv_half2<2, 3, 0>(o[2], o[3], vb, pa0_, pa1_); }
;         if (do1) { bf16x8 pa2_, pa3_; DS_PK4(p1, 0, pa2_); DS_PK4(p1, 8, pa3_);
;             pv_half2<0, 1, 1>(o[0], o[1], vb, pa2_, pa3_); pv_half2<2, 3, 1>(o[2], o[3], vb, pa2_, pa3_); }
.Lft1_noresc:
	v_permlane32_swap_b32_e32 v16, v18
	v_permlane32_swap_b32_e32 v17, v19
	v_permlane32_swap_b32_e32 v20, v22
	v_permlane32_swap_b32_e32 v21, v23
	v_pk_add_f32 v[0:1], v[0:1], v[70:71] neg_lo:[0,1] neg_hi:[0,1]
	v_pk_add_f32 v[2:3], v[2:3], v[70:71] neg_lo:[0,1] neg_hi:[0,1]
	v_pk_add_f32 v[4:5], v[4:5], v[70:71] neg_lo:[0,1] neg_hi:[0,1]
	v_pk_add_f32 v[6:7], v[6:7], v[70:71] neg_lo:[0,1] neg_hi:[0,1]
	v_pk_add_f32 v[8:9], v[8:9], v[70:71] neg_lo:[0,1] neg_hi:[0,1]
	v_pk_add_f32 v[10:11], v[10:11], v[70:71] neg_lo:[0,1] neg_hi:[0,1]
	v_pk_add_f32 v[12:13], v[12:13], v[70:71] neg_lo:[0,1] neg_hi:[0,1]
	v_pk_add_f32 v[14:15], v[14:15], v[70:71] neg_lo:[0,1] neg_hi:[0,1]
	v_exp_f32_e32 v0, v0
	v_exp_f32_e32 v1, v1
	v_exp_f32_e32 v2, v2
	v_exp_f32_e32 v3, v3
	v_exp_f32_e32 v4, v4
	v_exp_f32_e32 v5, v5
	v_exp_f32_e32 v6, v6
	v_exp_f32_e32 v7, v7
	v_exp_f32_e32 v8, v8
	v_exp_f32_e32 v9, v9
	v_exp_f32_e32 v10, v10
	v_exp_f32_e32 v11, v11
	v_exp_f32_e32 v12, v12
	v_exp_f32_e32 v13, v13
	v_exp_f32_e32 v14, v14
	v_exp_f32_e32 v15, v15
	v_pk_add_f32 v[74:75], v[74:75], v[0:1]
	v_pk_add_f32 v[74:75], v[74:75], v[2:3]
	v_pk_add_f32 v[74:75], v[74:75], v[4:5]
	v_pk_add_f32 v[74:75], v[74:75], v[6:7]
	v_pk_add_f32 v[74:75], v[74:75], v[8:9]
	v_pk_add_f32 v[74:75], v[74:75], v[10:11]
	v_pk_add_f32 v[74:75], v[74:75], v[12:13]
	v_pk_add_f32 v[74:75], v[74:75], v[14:15]
	v_add_f32_e32 v64, v74, v75
	s_waitcnt lgkmcnt(14)
	v_mfma_f32_32x32x16_bf16 v[80:95], v[16:19], v[32:35], v[80:95]
	ds_read_b64_tr_b16 v[32:33], v242 offset:8192
	s_waitcnt lgkmcnt(14)
	ds_read_b64_tr_b16 v[34:35], v242 offset:10240
	s_waitcnt lgkmcnt(14)
	v_mfma_f32_32x32x16_bf16 v[96:111], v[16:19], v[36:39], v[96:111]
	ds_read_b64_tr_b16 v[36:37], v242 offset:8704
	s_waitcnt lgkmcnt(14)
	ds_read_b64_tr_b16 v[38:39], v242 offset:10752
	s_waitcnt lgkmcnt(14)
	v_mfma_f32_32x32x16_bf16 v[80:95], v[20:23], v[40:43], v[80:95]
	ds_read_b64_tr_b16 v[40:41], v242 offset:12288
	s_waitcnt lgkmcnt(14)
	ds_read_b64_tr_b16 v[42:43], v242 offset:14336
	s_waitcnt lgkmcnt(14)
	v_mfma_f32_32x32x16_bf16 v[96:111], v[20:23], v[44:47], v[96:111]
	ds_read_b64_tr_b16 v[44:45], v242 offset:12800
	s_waitcnt lgkmcnt(14)
	ds_read_b64_tr_b16 v[46:47], v242 offset:14848
	s_waitcnt lgkmcnt(14)
	v_mfma_f32_32x32x16_bf16 v[112:127], v[16:19], v[48:51], v[112:127]
	ds_read_b64_tr_b16 v[48:49], v242 offset:9216
	s_waitcnt lgkmcnt(14)
	ds_read_b64_tr_b16 v[50:51], v242 offset:11264
	s_waitcnt lgkmcnt(14)
	v_mfma_f32_32x32x16_bf16 v[128:143], v[16:19], v[52:55], v[128:143]
	ds_read_b64_tr_b16 v[52:53], v242 offset:9728
	s_waitcnt lgkmcnt(14)
	ds_read_b64_tr_b16 v[54:55], v242 offset:11776
	s_waitcnt lgkmcnt(14)
	v_mfma_f32_32x32x16_bf16 v[112:127], v[20:23], v[56:59], v[112:127]
	ds_read_b64_tr_b16 v[56:57], v242 offset:13312
	s_waitcnt lgkmcnt(14)
	ds_read_b64_tr_b16 v[58:59], v242 offset:15360
	s_waitcnt lgkmcnt(14)
	v_mfma_f32_32x32x16_bf16 v[128:143], v[20:23], v[60:63], v[128:143]
	ds_read_b64_tr_b16 v[60:61], v242 offset:13824
	s_waitcnt lgkmcnt(14)
	ds_read_b64_tr_b16 v[62:63], v242 offset:15872
	v_cvt_pk_bf16_f32 v0, v0, v1
	v_cvt_pk_bf16_f32 v1, v2, v3
	v_cvt_pk_bf16_f32 v2, v4, v5
	v_cvt_pk_bf16_f32 v3, v6, v7
	v_cvt_pk_bf16_f32 v4, v8, v9
	v_cvt_pk_bf16_f32 v5, v10, v11
	v_cvt_pk_bf16_f32 v6, v12, v13
	v_cvt_pk_bf16_f32 v7, v14, v15
	v_mov_b32_e32 v67, v64
	v_permlane32_swap_b32_e32 v0, v2
	v_permlane32_swap_b32_e32 v1, v3
	v_permlane32_swap_b32_e32 v4, v6
	v_permlane32_swap_b32_e32 v5, v7
	v_permlane32_swap_b32_e32 v64, v67
	s_waitcnt lgkmcnt(14)
	v_mfma_f32_32x32x16_bf16 v[80:95], v[0:3], v[32:35], v[80:95]
	s_waitcnt lgkmcnt(12)
	v_mfma_f32_32x32x16_bf16 v[96:111], v[0:3], v[36:39], v[96:111]
	s_waitcnt lgkmcnt(10)
	v_mfma_f32_32x32x16_bf16 v[80:95], v[4:7], v[40:43], v[80:95]
	s_waitcnt lgkmcnt(8)
	v_mfma_f32_32x32x16_bf16 v[96:111], v[4:7], v[44:47], v[96:111]
	s_waitcnt lgkmcnt(6)
	v_mfma_f32_32x32x16_bf16 v[112:127], v[0:3], v[48:51], v[112:127]
	s_waitcnt lgkmcnt(4)
	v_mfma_f32_32x32x16_bf16 v[128:143], v[0:3], v[52:55], v[128:143]
	s_waitcnt lgkmcnt(2)
	v_mfma_f32_32x32x16_bf16 v[112:127], v[4:7], v[56:59], v[112:127]
	s_waitcnt lgkmcnt(0)
	v_mfma_f32_32x32x16_bf16 v[128:143], v[4:7], v[60:63], v[128:143]
	s_nop 1
	s_branch .LBB0_519
.Lft1_old:
	ds_read_b128 v[40:43], v0 offset:49152
	ds_read_b128 v[44:47], v38 offset:49152
	ds_read_b128 v[48:51], v37 offset:49152
	ds_read_b128 v[52:55], v36 offset:49152
	ds_read_b128 v[56:59], v35 offset:49152
	ds_read_b128 v[60:63], v34 offset:49152
	ds_read_b128 v[68:71], v33 offset:49152
	ds_read_b128 v[72:75], v32 offset:49152
	s_waitcnt lgkmcnt(7)
	v_mfma_f32_32x32x16_bf16 v[16:31], v[40:43], v[144:147], 0
	s_waitcnt lgkmcnt(6)
	v_mfma_f32_32x32x16_bf16 v[16:31], v[44:47], v[148:151], v[16:31]
	s_waitcnt lgkmcnt(5)
	v_mfma_f32_32x32x16_bf16 v[16:31], v[48:51], v[152:155], v[16:31]
	s_waitcnt lgkmcnt(4)
	v_mfma_f32_32x32x16_bf16 v[16:31], v[52:55], v[156:159], v[16:31]
	s_waitcnt lgkmcnt(3)
	v_mfma_f32_32x32x16_bf16 v[16:31], v[56:59], v[160:163], v[16:31]
	s_waitcnt lgkmcnt(2)
	v_mfma_f32_32x32x16_bf16 v[16:31], v[60:63], v[164:167], v[16:31]
	s_waitcnt lgkmcnt(1)
	v_mfma_f32_32x32x16_bf16 v[16:31], v[68:71], v[168:171], v[16:31]
	s_waitcnt lgkmcnt(0)
	v_mfma_f32_32x32x16_bf16 v[16:31], v[72:75], v[172:175], v[16:31]
	s_cmp_lg_u32 s12, 3
	s_cselect_b64 s[54:55], -1, 0
	s_cmp_eq_u32 s12, 3
	s_cbranch_scc0 .LBB0_490
